# routing phase: static s_setprio 1 for waves 4-7 as in the PEER expert phases
# speedup vs baseline: 1.0035x; 1.0026x over previous
.LBB0_665:
	s_or_b64 exec, exec, s[0:1]
	s_and_b64 s[0:1], s[30:31], exec
	s_movk_i32 s0, 0x410
	s_cselect_b32 s24, s0, 0x400
	v_readfirstlane_b32 s98, v0
	s_nop 3
	s_cmp_ge_u32 s98, 0x100
	s_cbranch_scc0 .Lpr_p9
	s_setprio 1
.Lpr_p9:
	v_mov_b32_e32 v51, v0
	s_cmp_ge_i32 s70, s24
	s_waitcnt lgkmcnt(0)
	s_barrier
	s_cbranch_scc1 .LBB0_673
	s_movk_i32 s0, 0x1000
	v_and_b32_e32 v2, 31, v51
	v_bfe_u32 v3, v51, 5, 1
	v_cmp_gt_i32_e64 s[38:39], s0, v51
	v_ashrrev_i32_e32 v4, 1, v51
	s_movk_i32 s0, 0xffe0
	v_bfi_b32 v56, s0, v4, v51
	v_lshl_add_u32 v4, v3, 4, 0
	v_lshlrev_b32_e32 v57, 2, v3
	v_mul_u32_u24_e32 v2, 0x90, v2
	s_lshl_b32 s25, s76, 10
	v_lshlrev_b32_e32 v50, 3, v3
	v_cmp_eq_u32_e64 s[40:41], 0, v3
	v_or_b32_e32 v58, 1, v57
	v_or_b32_e32 v59, 2, v57
	v_or_b32_e32 v60, 3, v57
	v_or_b32_e32 v61, 8, v57
	v_or_b32_e32 v62, 9, v57
	v_or_b32_e32 v63, 10, v57
	v_or_b32_e32 v64, 11, v57
	v_or_b32_e32 v65, 16, v57
	v_or_b32_e32 v66, 17, v57
	v_or_b32_e32 v67, 18, v57
	v_or_b32_e32 v68, 19, v57
	v_or_b32_e32 v69, 24, v57
	v_or_b32_e32 v70, 25, v57
	v_or_b32_e32 v71, 26, v57
	v_or_b32_e32 v72, 27, v57
	v_or_b32_e32 v73, 32, v57
	v_or_b32_e32 v74, 33, v57
	v_or_b32_e32 v75, 34, v57
	v_or_b32_e32 v76, 35, v57
	v_or_b32_e32 v77, 40, v57
	v_or_b32_e32 v78, 41, v57
	v_or_b32_e32 v79, 42, v57
	v_or_b32_e32 v80, 43, v57
	v_or_b32_e32 v81, 48, v57
	v_or_b32_e32 v82, 49, v57
	v_or_b32_e32 v83, 50, v57
	v_or_b32_e32 v84, 51, v57
	v_or_b32_e32 v85, 56, v57
	v_or_b32_e32 v86, 57, v57
	v_or_b32_e32 v87, 58, v57
	v_or_b32_e32 v88, 59, v57
	v_or_b32_e32 v89, 64, v57
	v_or_b32_e32 v90, 0x41, v57
	v_or_b32_e32 v91, 0x42, v57
	v_or_b32_e32 v92, 0x43, v57
	v_or_b32_e32 v93, 0x48, v57
	v_or_b32_e32 v94, 0x49, v57
	v_or_b32_e32 v95, 0x4a, v57
	v_or_b32_e32 v96, 0x4b, v57
	v_or_b32_e32 v97, 0x50, v57
	v_or_b32_e32 v98, 0x51, v57
	v_or_b32_e32 v99, 0x52, v57
	v_or_b32_e32 v100, 0x53, v57
	v_or_b32_e32 v101, 0x58, v57
	v_or_b32_e32 v102, 0x59, v57
	v_or_b32_e32 v103, 0x5a, v57
	v_or_b32_e32 v104, 0x5b, v57
	v_or_b32_e32 v105, 0x60, v57
	v_or_b32_e32 v106, 0x61, v57
	v_or_b32_e32 v107, 0x62, v57
	v_or_b32_e32 v108, 0x63, v57
	v_or_b32_e32 v109, 0x68, v57
	v_or_b32_e32 v110, 0x69, v57
	v_or_b32_e32 v111, 0x6a, v57
	v_or_b32_e32 v112, 0x6b, v57
	v_or_b32_e32 v113, 0x70, v57
	v_or_b32_e32 v114, 0x71, v57
	v_or_b32_e32 v115, 0x72, v57
	v_or_b32_e32 v116, 0x73, v57
	v_or_b32_e32 v117, 0x78, v57
	v_or_b32_e32 v118, 0x79, v57
	v_or_b32_e32 v119, 0x7a, v57
	v_or_b32_e32 v120, 0x7b, v57
	v_lshlrev_b32_e32 v121, 2, v51
	s_mov_b32 s0, -1
	v_add_u32_e32 v122, v4, v2
	s_mov_b32 s34, s70
	s_branch .LBB0_669

.LBB0_673:
	s_setprio 0
	s_waitcnt vmcnt(0)
	s_barrier
	s_and_saveexec_b64 s[0:1], s[44:45]
	s_cbranch_execz .LBB0_721
	v_readlane_b32 s2, v255, 29
	s_waitcnt vmcnt(0) expcnt(0) lgkmcnt(0)
	s_nop 0
	v_mov_b32_e32 v2, s2
	ds_read_b32 v4, v2
	v_readlane_b32 s2, v255, 30
	s_waitcnt lgkmcnt(0)
	v_cmp_ne_u32_e32 vcc, 0, v4
	v_mov_b32_e32 v2, s2
	ds_read_b32 v2, v2
	s_cbranch_vccnz .LBB0_689
	v_readlane_b32 s4, v253, 16
	v_readlane_b32 s5, v253, 17
	s_load_dwordx2 s[2:3], s[4:5], 0x4
	s_waitcnt lgkmcnt(0)
	s_mul_i32 s2, s2, s86
	s_mul_i32 s2, s2, s3
	s_mov_b32 s3, 1
	s_branch .LBB0_677
